# conv quota rebalanced 157/237 tiles + hand-pipelined P11 combine loop (two tokens in flight, lane-parallel index loads)
# speedup vs baseline: 1.0248x; 1.0055x over previous
.Lconv_entry:
	v_readlane_b32 s0, v255, 7
	s_and_b32 s1, s76, 31
	s_lshl_b32 s1, s1, 3
	s_lshr_b32 s2, s76, 5
	s_or_b32 s1, s1, s2
	s_mul_i32 s2, s1, 0x9d
	s_sub_u32 s3, s1, 0x90
	s_mul_i32 s3, s3, 0xed
	s_add_u32 s3, s3, 0x5850
	s_movk_i32 s15, 0xed
	s_cmp_lt_u32 s1, 0x90
	s_cselect_b32 s14, s2, s3
	s_cselect_b32 s15, 0x9d, s15
	s_add_u32 s15, s15, s14
	s_add_u32 s14, s14, s0
	v_lshrrev_b32_e32 v2, 3, v254
	v_lshlrev_b32_e32 v2, 4, v2
	v_and_b32_e32 v3, 7, v254
	v_lshlrev_b32_e32 v4, 4, v3
	v_lshlrev_b32_e32 v3, 2, v3
	v_mov_b32_e32 v5, 0x43e00000
	s_mov_b32 s25, 0xc3e00000
	s_cmp_lt_u32 s14, s15
	s_cbranch_scc0 .Lconv_done
	s_cmp_lt_u32 s14, 0x8000
	s_cbranch_scc0 .Lconv_dn_p
	s_lshr_b32 s0, s14, 14
	s_and_b32 s1, s14, 0x3fff
	s_cmp_eq_u32 s0, 0
	s_cselect_b32 s16, s36, s38
	s_cselect_b32 s17, s37, s39
	s_lshr_b32 s2, s1, 8
	s_and_b32 s3, s1, 0xff
	s_lshr_b32 s1, s3, 4
	s_and_b32 s3, s3, 15
	s_lshl_b32 s10, s2, 22
	s_lshl_b32 s11, s1, 18
	s_add_u32 s10, s10, s11
	s_lshl_b32 s11, s3, 7
	s_add_u32 s10, s10, s11
	s_add_u32 s16, s16, s10
	s_addc_u32 s17, s17, 0
	s_movk_i32 s18, 0x800
	s_lshl_b32 s10, s2, 10
	s_lshr_b32 s11, s3, 2
	s_lshl_b32 s11, s11, 8
	s_add_u32 s10, s10, s11
	s_lshl_b32 s11, s0, 7
	s_add_u32 s10, s10, s11
	s_and_b32 s11, s3, 3
	s_lshl_b32 s11, s11, 5
	s_add_u32 s10, s10, s11
	s_lshl_b32 s10, s10, 11
	s_lshl_b32 s11, s1, 7
	s_add_u32 s10, s10, s11
	s_add_u32 s20, s50, 0x1c200000
	s_addc_u32 s21, s51, 0
	s_add_u32 s20, s20, s10
	s_addc_u32 s21, s21, 0
	s_movk_i32 s19, 0x800
	s_branch .Lconv_ad_p

.LBB0_2174:
	s_lshl_b32 s0, s76, 3
	v_readlane_b32 s1, v255, 7
	s_add_i32 s0, s0, s1
	s_cmpk_gt_i32 s0, 0x1fff
	s_waitcnt lgkmcnt(0)
	s_barrier
	s_cbranch_scc1 .LBB0_2177
	v_lshlrev_b32_e32 v0, 4, v254
	v_lshlrev_b32_e32 v1, 5, v254
	v_lshlrev_b32_e32 v2, 6, v254
	v_and_b32_e32 v3, 7, v254
	v_lshlrev_b32_e32 v3, 2, v3
	s_mov_b32 s52, s0
	s_lshl_b32 s53, s33, 3
	s_add_u32 s54, s50, 0x200000
	s_addc_u32 s55, s51, 0
	s_add_u32 s56, s50, 0x280000
	s_addc_u32 s57, s51, 0
	s_add_u32 s58, s50, 0x240000
	s_addc_u32 s59, s51, 0
	s_add_u32 s60, s50, 0x400000
	s_addc_u32 s61, s51, 0
	s_add_u32 s62, s50, 0x3c000000
	s_addc_u32 s63, s51, 0
	s_add_u32 s64, s95, 0xa000
	s_addc_u32 s65, s96, 0
	s_mov_b32 s66, s52
	s_lshl_b32 s66, s66, 5
	s_add_u32 s68, s54, s66
	s_addc_u32 s69, s55, 0
	global_load_dword v4, v3, s[68:69]
	s_add_u32 s68, s56, s66
	s_addc_u32 s69, s57, 0
	global_load_dword v5, v3, s[68:69]
	s_add_u32 s68, s58, s66
	s_addc_u32 s69, s59, 0
	global_load_dword v6, v3, s[68:69]
	s_waitcnt vmcnt(0)
	v_lshlrev_b32_e32 v7, 2, v4
	v_add_u32_e32 v7, 0x21540, v7
	ds_read_b32 v7, v7
	s_waitcnt lgkmcnt(0)
	v_add_u32_e32 v7, v7, v5
	s_nop 1
	v_readlane_b32 s70, v7, 0
	v_readlane_b32 s71, v7, 1
	v_readlane_b32 s72, v7, 2
	v_readlane_b32 s73, v7, 3
	v_readlane_b32 s74, v7, 4
	v_readlane_b32 s75, v7, 5
	v_readlane_b32 s76, v7, 6
	v_readlane_b32 s77, v7, 7
	v_readlane_b32 s0, v6, 0
	v_readlane_b32 s2, v6, 1
	v_readlane_b32 s4, v6, 2
	v_readlane_b32 s6, v6, 3
	v_readlane_b32 s8, v6, 4
	v_readlane_b32 s10, v6, 5
	v_readlane_b32 s12, v6, 6
	v_readlane_b32 s14, v6, 7
	s_mov_b32 s66, s52
	s_lshl_b32 s67, s66, 12
	s_add_u32 s68, s62, s67
	s_addc_u32 s69, s63, 0
	global_load_dwordx4 v[88:91], v1, s[68:69] nt
	global_load_dwordx4 v[92:95], v1, s[68:69] offset:16 nt
	global_load_dwordx4 v[96:99], v1, s[68:69] offset:2048 nt
	global_load_dwordx4 v[100:103], v1, s[68:69] offset:2064 nt
	s_add_u32 s67, s66, 0x10000
	s_lshl_b32 s67, s67, 11
	s_add_u32 s68, s60, s67
	s_addc_u32 s69, s61, 0
	global_load_dwordx4 v[16:19], v0, s[68:69] nt
	global_load_dwordx4 v[20:23], v0, s[68:69] offset:1024 nt
	s_lshl_b32 s67, s70, 11
	s_add_u32 s68, s60, s67
	s_addc_u32 s69, s61, 0
	global_load_dwordx4 v[24:27], v0, s[68:69] nt
	global_load_dwordx4 v[28:31], v0, s[68:69] offset:1024 nt
	s_lshl_b32 s67, s71, 11
	s_add_u32 s68, s60, s67
	s_addc_u32 s69, s61, 0
	global_load_dwordx4 v[32:35], v0, s[68:69] nt
	global_load_dwordx4 v[36:39], v0, s[68:69] offset:1024 nt
	s_lshl_b32 s67, s72, 11
	s_add_u32 s68, s60, s67
	s_addc_u32 s69, s61, 0
	global_load_dwordx4 v[40:43], v0, s[68:69] nt
	global_load_dwordx4 v[44:47], v0, s[68:69] offset:1024 nt
	s_lshl_b32 s67, s73, 11
	s_add_u32 s68, s60, s67
	s_addc_u32 s69, s61, 0
	global_load_dwordx4 v[48:51], v0, s[68:69] nt
	global_load_dwordx4 v[52:55], v0, s[68:69] offset:1024 nt
	s_lshl_b32 s67, s74, 11
	s_add_u32 s68, s60, s67
	s_addc_u32 s69, s61, 0
	global_load_dwordx4 v[56:59], v0, s[68:69] nt
	global_load_dwordx4 v[60:63], v0, s[68:69] offset:1024 nt
	s_lshl_b32 s67, s75, 11
	s_add_u32 s68, s60, s67
	s_addc_u32 s69, s61, 0
	global_load_dwordx4 v[64:67], v0, s[68:69] nt
	global_load_dwordx4 v[68:71], v0, s[68:69] offset:1024 nt
	s_lshl_b32 s67, s76, 11
	s_add_u32 s68, s60, s67
	s_addc_u32 s69, s61, 0
	global_load_dwordx4 v[72:75], v0, s[68:69] nt
	global_load_dwordx4 v[76:79], v0, s[68:69] offset:1024 nt
	s_lshl_b32 s67, s77, 11
	s_add_u32 s68, s60, s67
	s_addc_u32 s69, s61, 0
	global_load_dwordx4 v[80:83], v0, s[68:69] nt
	global_load_dwordx4 v[84:87], v0, s[68:69] offset:1024 nt
	s_mov_b32 s66, s52
	s_lshr_b32 s67, s66, 12
	s_mul_i32 s67, s67, 0xc000
	s_add_u32 s68, s64, s67
	s_addc_u32 s69, s65, 0
	global_load_dwordx4 v[192:195], v2, s[68:69]
	global_load_dwordx4 v[196:199], v2, s[68:69] offset:16
	global_load_dwordx4 v[200:203], v2, s[68:69] offset:32
	global_load_dwordx4 v[204:207], v2, s[68:69] offset:48
	s_add_u32 s68, s68, 0x1000
	s_addc_u32 s69, s69, 0
	global_load_dwordx4 v[208:211], v2, s[68:69]
	global_load_dwordx4 v[212:215], v2, s[68:69] offset:16
	global_load_dwordx4 v[216:219], v2, s[68:69] offset:32
	global_load_dwordx4 v[220:223], v2, s[68:69] offset:48
	s_add_u32 s78, s52, s53
	s_add_u32 s79, s78, s53
	s_cmp_lt_u32 s78, 0x2000
	s_cbranch_scc0 .Lcomb_sk0
	s_mov_b32 s66, s78
	s_lshl_b32 s66, s66, 5
	s_add_u32 s68, s54, s66
	s_addc_u32 s69, s55, 0
	global_load_dword v4, v3, s[68:69]
	s_add_u32 s68, s56, s66
	s_addc_u32 s69, s57, 0
	global_load_dword v5, v3, s[68:69]
	s_add_u32 s68, s58, s66
	s_addc_u32 s69, s59, 0
	global_load_dword v6, v3, s[68:69]
.Lcomb_sk0:
	s_waitcnt vmcnt(0)
	s_cmp_lt_u32 s78, 0x2000
	s_cbranch_scc0 .Lcomb_sk1
	v_lshlrev_b32_e32 v7, 2, v4
	v_add_u32_e32 v7, 0x21540, v7
	ds_read_b32 v7, v7
	s_waitcnt lgkmcnt(0)
	v_add_u32_e32 v7, v7, v5
	s_nop 1
	v_readlane_b32 s70, v7, 0
	v_readlane_b32 s71, v7, 1
	v_readlane_b32 s72, v7, 2
	v_readlane_b32 s73, v7, 3
	v_readlane_b32 s74, v7, 4
	v_readlane_b32 s75, v7, 5
	v_readlane_b32 s76, v7, 6
	v_readlane_b32 s77, v7, 7
	v_readlane_b32 s16, v6, 0
	v_readlane_b32 s18, v6, 1
	v_readlane_b32 s20, v6, 2
	v_readlane_b32 s22, v6, 3
	v_readlane_b32 s24, v6, 4
	v_readlane_b32 s26, v6, 5
	v_readlane_b32 s28, v6, 6
	v_readlane_b32 s30, v6, 7
	s_mov_b32 s66, s78
	s_lshl_b32 s67, s66, 12
	s_add_u32 s68, s62, s67
	s_addc_u32 s69, s63, 0
	global_load_dwordx4 v[176:179], v1, s[68:69] nt
	global_load_dwordx4 v[180:183], v1, s[68:69] offset:16 nt
	global_load_dwordx4 v[184:187], v1, s[68:69] offset:2048 nt
	global_load_dwordx4 v[188:191], v1, s[68:69] offset:2064 nt
	s_add_u32 s67, s66, 0x10000
	s_lshl_b32 s67, s67, 11
	s_add_u32 s68, s60, s67
	s_addc_u32 s69, s61, 0
	global_load_dwordx4 v[104:107], v0, s[68:69] nt
	global_load_dwordx4 v[108:111], v0, s[68:69] offset:1024 nt
	s_lshl_b32 s67, s70, 11
	s_add_u32 s68, s60, s67
	s_addc_u32 s69, s61, 0
	global_load_dwordx4 v[112:115], v0, s[68:69] nt
	global_load_dwordx4 v[116:119], v0, s[68:69] offset:1024 nt
	s_lshl_b32 s67, s71, 11
	s_add_u32 s68, s60, s67
	s_addc_u32 s69, s61, 0
	global_load_dwordx4 v[120:123], v0, s[68:69] nt
	global_load_dwordx4 v[124:127], v0, s[68:69] offset:1024 nt
	s_lshl_b32 s67, s72, 11
	s_add_u32 s68, s60, s67
	s_addc_u32 s69, s61, 0
	global_load_dwordx4 v[128:131], v0, s[68:69] nt
	global_load_dwordx4 v[132:135], v0, s[68:69] offset:1024 nt
	s_lshl_b32 s67, s73, 11
	s_add_u32 s68, s60, s67
	s_addc_u32 s69, s61, 0
	global_load_dwordx4 v[136:139], v0, s[68:69] nt
	global_load_dwordx4 v[140:143], v0, s[68:69] offset:1024 nt
	s_lshl_b32 s67, s74, 11
	s_add_u32 s68, s60, s67
	s_addc_u32 s69, s61, 0
	global_load_dwordx4 v[144:147], v0, s[68:69] nt
	global_load_dwordx4 v[148:151], v0, s[68:69] offset:1024 nt
	s_lshl_b32 s67, s75, 11
	s_add_u32 s68, s60, s67
	s_addc_u32 s69, s61, 0
	global_load_dwordx4 v[152:155], v0, s[68:69] nt
	global_load_dwordx4 v[156:159], v0, s[68:69] offset:1024 nt
	s_lshl_b32 s67, s76, 11
	s_add_u32 s68, s60, s67
	s_addc_u32 s69, s61, 0
	global_load_dwordx4 v[160:163], v0, s[68:69] nt
	global_load_dwordx4 v[164:167], v0, s[68:69] offset:1024 nt
	s_lshl_b32 s67, s77, 11
	s_add_u32 s68, s60, s67
	s_addc_u32 s69, s61, 0
	global_load_dwordx4 v[168:171], v0, s[68:69] nt
	global_load_dwordx4 v[172:175], v0, s[68:69] offset:1024 nt
.Lcomb_sk1:
	s_cmp_lt_u32 s79, 0x2000
	s_cbranch_scc0 .Lcomb_sk2
	s_mov_b32 s66, s79
	s_lshl_b32 s66, s66, 5
	s_add_u32 s68, s54, s66
	s_addc_u32 s69, s55, 0
	global_load_dword v4, v3, s[68:69]
	s_add_u32 s68, s56, s66
	s_addc_u32 s69, s57, 0
	global_load_dword v5, v3, s[68:69]
	s_add_u32 s68, s58, s66
	s_addc_u32 s69, s59, 0
	global_load_dword v6, v3, s[68:69]
.Lcomb_sk2:
.Lcomb_loop:
	s_lshl_b32 s67, s52, 13
	s_add_u32 s68, s48, s67
	s_addc_u32 s69, s49, 0
	v_cvt_pk_f32_fp8_e32 v[224:225], v16
	v_cvt_pk_f32_fp8_sdwa v[226:227], v16 src0_sel:WORD_1
	v_cvt_pk_f32_fp8_e32 v[228:229], v17
	v_cvt_pk_f32_fp8_sdwa v[230:231], v17 src0_sel:WORD_1
	v_cvt_pk_f32_fp8_e32 v[232:233], v18
	v_cvt_pk_f32_fp8_sdwa v[234:235], v18 src0_sel:WORD_1
	v_cvt_pk_f32_fp8_e32 v[236:237], v19
	v_cvt_pk_f32_fp8_sdwa v[238:239], v19 src0_sel:WORD_1
	v_cvt_pk_f32_fp8_e32 v[8:9], v24
	v_cvt_pk_f32_fp8_sdwa v[10:11], v24 src0_sel:WORD_1
	v_pk_fma_f32 v[224:225], v[8:9], s[0:1], v[224:225] op_sel_hi:[1,0,1]
	v_pk_fma_f32 v[226:227], v[10:11], s[0:1], v[226:227] op_sel_hi:[1,0,1]
	v_cvt_pk_f32_fp8_e32 v[12:13], v25
	v_cvt_pk_f32_fp8_sdwa v[14:15], v25 src0_sel:WORD_1
	v_pk_fma_f32 v[228:229], v[12:13], s[0:1], v[228:229] op_sel_hi:[1,0,1]
	v_pk_fma_f32 v[230:231], v[14:15], s[0:1], v[230:231] op_sel_hi:[1,0,1]
	v_cvt_pk_f32_fp8_e32 v[8:9], v26
	v_cvt_pk_f32_fp8_sdwa v[10:11], v26 src0_sel:WORD_1
	v_pk_fma_f32 v[232:233], v[8:9], s[0:1], v[232:233] op_sel_hi:[1,0,1]
	v_pk_fma_f32 v[234:235], v[10:11], s[0:1], v[234:235] op_sel_hi:[1,0,1]
	v_cvt_pk_f32_fp8_e32 v[12:13], v27
	v_cvt_pk_f32_fp8_sdwa v[14:15], v27 src0_sel:WORD_1
	v_pk_fma_f32 v[236:237], v[12:13], s[0:1], v[236:237] op_sel_hi:[1,0,1]
	v_pk_fma_f32 v[238:239], v[14:15], s[0:1], v[238:239] op_sel_hi:[1,0,1]
	v_cvt_pk_f32_fp8_e32 v[8:9], v32
	v_cvt_pk_f32_fp8_sdwa v[10:11], v32 src0_sel:WORD_1
	v_pk_fma_f32 v[224:225], v[8:9], s[2:3], v[224:225] op_sel_hi:[1,0,1]
	v_pk_fma_f32 v[226:227], v[10:11], s[2:3], v[226:227] op_sel_hi:[1,0,1]
	v_cvt_pk_f32_fp8_e32 v[12:13], v33
	v_cvt_pk_f32_fp8_sdwa v[14:15], v33 src0_sel:WORD_1
	v_pk_fma_f32 v[228:229], v[12:13], s[2:3], v[228:229] op_sel_hi:[1,0,1]
	v_pk_fma_f32 v[230:231], v[14:15], s[2:3], v[230:231] op_sel_hi:[1,0,1]
	v_cvt_pk_f32_fp8_e32 v[8:9], v34
	v_cvt_pk_f32_fp8_sdwa v[10:11], v34 src0_sel:WORD_1
	v_pk_fma_f32 v[232:233], v[8:9], s[2:3], v[232:233] op_sel_hi:[1,0,1]
	v_pk_fma_f32 v[234:235], v[10:11], s[2:3], v[234:235] op_sel_hi:[1,0,1]
	v_cvt_pk_f32_fp8_e32 v[12:13], v35
	v_cvt_pk_f32_fp8_sdwa v[14:15], v35 src0_sel:WORD_1
	v_pk_fma_f32 v[236:237], v[12:13], s[2:3], v[236:237] op_sel_hi:[1,0,1]
	v_pk_fma_f32 v[238:239], v[14:15], s[2:3], v[238:239] op_sel_hi:[1,0,1]
	v_cvt_pk_f32_fp8_e32 v[8:9], v40
	v_cvt_pk_f32_fp8_sdwa v[10:11], v40 src0_sel:WORD_1
	v_pk_fma_f32 v[224:225], v[8:9], s[4:5], v[224:225] op_sel_hi:[1,0,1]
	v_pk_fma_f32 v[226:227], v[10:11], s[4:5], v[226:227] op_sel_hi:[1,0,1]
	v_cvt_pk_f32_fp8_e32 v[12:13], v41
	v_cvt_pk_f32_fp8_sdwa v[14:15], v41 src0_sel:WORD_1
	v_pk_fma_f32 v[228:229], v[12:13], s[4:5], v[228:229] op_sel_hi:[1,0,1]
	v_pk_fma_f32 v[230:231], v[14:15], s[4:5], v[230:231] op_sel_hi:[1,0,1]
	v_cvt_pk_f32_fp8_e32 v[8:9], v42
	v_cvt_pk_f32_fp8_sdwa v[10:11], v42 src0_sel:WORD_1
	v_pk_fma_f32 v[232:233], v[8:9], s[4:5], v[232:233] op_sel_hi:[1,0,1]
	v_pk_fma_f32 v[234:235], v[10:11], s[4:5], v[234:235] op_sel_hi:[1,0,1]
	v_cvt_pk_f32_fp8_e32 v[12:13], v43
	v_cvt_pk_f32_fp8_sdwa v[14:15], v43 src0_sel:WORD_1
	v_pk_fma_f32 v[236:237], v[12:13], s[4:5], v[236:237] op_sel_hi:[1,0,1]
	v_pk_fma_f32 v[238:239], v[14:15], s[4:5], v[238:239] op_sel_hi:[1,0,1]
	v_cvt_pk_f32_fp8_e32 v[8:9], v48
	v_cvt_pk_f32_fp8_sdwa v[10:11], v48 src0_sel:WORD_1
	v_pk_fma_f32 v[224:225], v[8:9], s[6:7], v[224:225] op_sel_hi:[1,0,1]
	v_pk_fma_f32 v[226:227], v[10:11], s[6:7], v[226:227] op_sel_hi:[1,0,1]
	v_cvt_pk_f32_fp8_e32 v[12:13], v49
	v_cvt_pk_f32_fp8_sdwa v[14:15], v49 src0_sel:WORD_1
	v_pk_fma_f32 v[228:229], v[12:13], s[6:7], v[228:229] op_sel_hi:[1,0,1]
	v_pk_fma_f32 v[230:231], v[14:15], s[6:7], v[230:231] op_sel_hi:[1,0,1]
	v_cvt_pk_f32_fp8_e32 v[8:9], v50
	v_cvt_pk_f32_fp8_sdwa v[10:11], v50 src0_sel:WORD_1
	v_pk_fma_f32 v[232:233], v[8:9], s[6:7], v[232:233] op_sel_hi:[1,0,1]
	v_pk_fma_f32 v[234:235], v[10:11], s[6:7], v[234:235] op_sel_hi:[1,0,1]
	v_cvt_pk_f32_fp8_e32 v[12:13], v51
	v_cvt_pk_f32_fp8_sdwa v[14:15], v51 src0_sel:WORD_1
	v_pk_fma_f32 v[236:237], v[12:13], s[6:7], v[236:237] op_sel_hi:[1,0,1]
	v_pk_fma_f32 v[238:239], v[14:15], s[6:7], v[238:239] op_sel_hi:[1,0,1]
	v_cvt_pk_f32_fp8_e32 v[8:9], v56
	v_cvt_pk_f32_fp8_sdwa v[10:11], v56 src0_sel:WORD_1
	v_pk_fma_f32 v[224:225], v[8:9], s[8:9], v[224:225] op_sel_hi:[1,0,1]
	v_pk_fma_f32 v[226:227], v[10:11], s[8:9], v[226:227] op_sel_hi:[1,0,1]
	v_cvt_pk_f32_fp8_e32 v[12:13], v57
	v_cvt_pk_f32_fp8_sdwa v[14:15], v57 src0_sel:WORD_1
	v_pk_fma_f32 v[228:229], v[12:13], s[8:9], v[228:229] op_sel_hi:[1,0,1]
	v_pk_fma_f32 v[230:231], v[14:15], s[8:9], v[230:231] op_sel_hi:[1,0,1]
	v_cvt_pk_f32_fp8_e32 v[8:9], v58
	v_cvt_pk_f32_fp8_sdwa v[10:11], v58 src0_sel:WORD_1
	v_pk_fma_f32 v[232:233], v[8:9], s[8:9], v[232:233] op_sel_hi:[1,0,1]
	v_pk_fma_f32 v[234:235], v[10:11], s[8:9], v[234:235] op_sel_hi:[1,0,1]
	v_cvt_pk_f32_fp8_e32 v[12:13], v59
	v_cvt_pk_f32_fp8_sdwa v[14:15], v59 src0_sel:WORD_1
	v_pk_fma_f32 v[236:237], v[12:13], s[8:9], v[236:237] op_sel_hi:[1,0,1]
	v_pk_fma_f32 v[238:239], v[14:15], s[8:9], v[238:239] op_sel_hi:[1,0,1]
	v_cvt_pk_f32_fp8_e32 v[8:9], v64
	v_cvt_pk_f32_fp8_sdwa v[10:11], v64 src0_sel:WORD_1
	v_pk_fma_f32 v[224:225], v[8:9], s[10:11], v[224:225] op_sel_hi:[1,0,1]
	v_pk_fma_f32 v[226:227], v[10:11], s[10:11], v[226:227] op_sel_hi:[1,0,1]
	v_cvt_pk_f32_fp8_e32 v[12:13], v65
	v_cvt_pk_f32_fp8_sdwa v[14:15], v65 src0_sel:WORD_1
	v_pk_fma_f32 v[228:229], v[12:13], s[10:11], v[228:229] op_sel_hi:[1,0,1]
	v_pk_fma_f32 v[230:231], v[14:15], s[10:11], v[230:231] op_sel_hi:[1,0,1]
	v_cvt_pk_f32_fp8_e32 v[8:9], v66
	v_cvt_pk_f32_fp8_sdwa v[10:11], v66 src0_sel:WORD_1
	v_pk_fma_f32 v[232:233], v[8:9], s[10:11], v[232:233] op_sel_hi:[1,0,1]
	v_pk_fma_f32 v[234:235], v[10:11], s[10:11], v[234:235] op_sel_hi:[1,0,1]
	v_cvt_pk_f32_fp8_e32 v[12:13], v67
	v_cvt_pk_f32_fp8_sdwa v[14:15], v67 src0_sel:WORD_1
	v_pk_fma_f32 v[236:237], v[12:13], s[10:11], v[236:237] op_sel_hi:[1,0,1]
	v_pk_fma_f32 v[238:239], v[14:15], s[10:11], v[238:239] op_sel_hi:[1,0,1]
	v_cvt_pk_f32_fp8_e32 v[8:9], v72
	v_cvt_pk_f32_fp8_sdwa v[10:11], v72 src0_sel:WORD_1
	v_pk_fma_f32 v[224:225], v[8:9], s[12:13], v[224:225] op_sel_hi:[1,0,1]
	v_pk_fma_f32 v[226:227], v[10:11], s[12:13], v[226:227] op_sel_hi:[1,0,1]
	v_cvt_pk_f32_fp8_e32 v[12:13], v73
	v_cvt_pk_f32_fp8_sdwa v[14:15], v73 src0_sel:WORD_1
	v_pk_fma_f32 v[228:229], v[12:13], s[12:13], v[228:229] op_sel_hi:[1,0,1]
	v_pk_fma_f32 v[230:231], v[14:15], s[12:13], v[230:231] op_sel_hi:[1,0,1]
	v_cvt_pk_f32_fp8_e32 v[8:9], v74
	v_cvt_pk_f32_fp8_sdwa v[10:11], v74 src0_sel:WORD_1
	v_pk_fma_f32 v[232:233], v[8:9], s[12:13], v[232:233] op_sel_hi:[1,0,1]
	v_pk_fma_f32 v[234:235], v[10:11], s[12:13], v[234:235] op_sel_hi:[1,0,1]
	v_cvt_pk_f32_fp8_e32 v[12:13], v75
	v_cvt_pk_f32_fp8_sdwa v[14:15], v75 src0_sel:WORD_1
	v_pk_fma_f32 v[236:237], v[12:13], s[12:13], v[236:237] op_sel_hi:[1,0,1]
	v_pk_fma_f32 v[238:239], v[14:15], s[12:13], v[238:239] op_sel_hi:[1,0,1]
	v_cvt_pk_f32_fp8_e32 v[8:9], v80
	v_cvt_pk_f32_fp8_sdwa v[10:11], v80 src0_sel:WORD_1
	v_pk_fma_f32 v[224:225], v[8:9], s[14:15], v[224:225] op_sel_hi:[1,0,1]
	v_pk_fma_f32 v[226:227], v[10:11], s[14:15], v[226:227] op_sel_hi:[1,0,1]
	v_cvt_pk_f32_fp8_e32 v[12:13], v81
	v_cvt_pk_f32_fp8_sdwa v[14:15], v81 src0_sel:WORD_1
	v_pk_fma_f32 v[228:229], v[12:13], s[14:15], v[228:229] op_sel_hi:[1,0,1]
	v_pk_fma_f32 v[230:231], v[14:15], s[14:15], v[230:231] op_sel_hi:[1,0,1]
	v_cvt_pk_f32_fp8_e32 v[8:9], v82
	v_cvt_pk_f32_fp8_sdwa v[10:11], v82 src0_sel:WORD_1
	v_pk_fma_f32 v[232:233], v[8:9], s[14:15], v[232:233] op_sel_hi:[1,0,1]
	v_pk_fma_f32 v[234:235], v[10:11], s[14:15], v[234:235] op_sel_hi:[1,0,1]
	v_cvt_pk_f32_fp8_e32 v[12:13], v83
	v_cvt_pk_f32_fp8_sdwa v[14:15], v83 src0_sel:WORD_1
	v_pk_fma_f32 v[236:237], v[12:13], s[14:15], v[236:237] op_sel_hi:[1,0,1]
	v_pk_fma_f32 v[238:239], v[14:15], s[14:15], v[238:239] op_sel_hi:[1,0,1]
	v_lshlrev_b32_e32 v240, 16, v88
	v_and_b32_e32 v241, 0xffff0000, v88
	v_lshlrev_b32_e32 v242, 16, v89
	v_and_b32_e32 v243, 0xffff0000, v89
	v_lshlrev_b32_e32 v244, 16, v90
	v_and_b32_e32 v245, 0xffff0000, v90
	v_lshlrev_b32_e32 v246, 16, v91
	v_and_b32_e32 v247, 0xffff0000, v91
	v_lshlrev_b32_e32 v248, 16, v92
	v_and_b32_e32 v249, 0xffff0000, v92
	v_lshlrev_b32_e32 v250, 16, v93
	v_and_b32_e32 v251, 0xffff0000, v93
	v_lshlrev_b32_e32 v252, 16, v94
	v_and_b32_e32 v253, 0xffff0000, v94
	v_lshlrev_b32_e32 v254, 16, v95
	v_and_b32_e32 v255, 0xffff0000, v95
	s_cmp_lt_u32 s79, 0x2000
	s_cbranch_scc0 .Lcomb_wa3
	s_waitcnt vmcnt(25)
	s_branch .Lcomb_wj3
.Lcomb_wa3:
	s_cmp_lt_u32 s78, 0x2000
	s_cbranch_scc0 .Lcomb_wb3
	s_waitcnt vmcnt(22)
	s_branch .Lcomb_wj3

.Lcomb_wj3:
	v_pk_fma_f32 v[240:241], v[224:225], v[192:193], v[240:241]
	v_pk_fma_f32 v[242:243], v[226:227], v[194:195], v[242:243]
	v_pk_fma_f32 v[244:245], v[228:229], v[196:197], v[244:245]
	v_pk_fma_f32 v[246:247], v[230:231], v[198:199], v[246:247]
	v_pk_fma_f32 v[248:249], v[232:233], v[200:201], v[248:249]
	v_pk_fma_f32 v[250:251], v[234:235], v[202:203], v[250:251]
	v_pk_fma_f32 v[252:253], v[236:237], v[204:205], v[252:253]
	v_pk_fma_f32 v[254:255], v[238:239], v[206:207], v[254:255]
	global_store_dwordx4 v2, v[240:243], s[68:69]
	global_store_dwordx4 v2, v[244:247], s[68:69] offset:16
	global_store_dwordx4 v2, v[248:251], s[68:69] offset:32
	global_store_dwordx4 v2, v[252:255], s[68:69] offset:48
	s_add_u32 s68, s68, 0x1000
	s_addc_u32 s69, s69, 0
	v_cvt_pk_f32_fp8_e32 v[224:225], v20
	v_cvt_pk_f32_fp8_sdwa v[226:227], v20 src0_sel:WORD_1
	v_cvt_pk_f32_fp8_e32 v[228:229], v21
	v_cvt_pk_f32_fp8_sdwa v[230:231], v21 src0_sel:WORD_1
	v_cvt_pk_f32_fp8_e32 v[232:233], v22
	v_cvt_pk_f32_fp8_sdwa v[234:235], v22 src0_sel:WORD_1
	v_cvt_pk_f32_fp8_e32 v[236:237], v23
	v_cvt_pk_f32_fp8_sdwa v[238:239], v23 src0_sel:WORD_1
	v_cvt_pk_f32_fp8_e32 v[8:9], v28
	v_cvt_pk_f32_fp8_sdwa v[10:11], v28 src0_sel:WORD_1
	v_pk_fma_f32 v[224:225], v[8:9], s[0:1], v[224:225] op_sel_hi:[1,0,1]
	v_pk_fma_f32 v[226:227], v[10:11], s[0:1], v[226:227] op_sel_hi:[1,0,1]
	v_cvt_pk_f32_fp8_e32 v[12:13], v29
	v_cvt_pk_f32_fp8_sdwa v[14:15], v29 src0_sel:WORD_1
	v_pk_fma_f32 v[228:229], v[12:13], s[0:1], v[228:229] op_sel_hi:[1,0,1]
	v_pk_fma_f32 v[230:231], v[14:15], s[0:1], v[230:231] op_sel_hi:[1,0,1]
	v_cvt_pk_f32_fp8_e32 v[8:9], v30
	v_cvt_pk_f32_fp8_sdwa v[10:11], v30 src0_sel:WORD_1
	v_pk_fma_f32 v[232:233], v[8:9], s[0:1], v[232:233] op_sel_hi:[1,0,1]
	v_pk_fma_f32 v[234:235], v[10:11], s[0:1], v[234:235] op_sel_hi:[1,0,1]
	v_cvt_pk_f32_fp8_e32 v[12:13], v31
	v_cvt_pk_f32_fp8_sdwa v[14:15], v31 src0_sel:WORD_1
	v_pk_fma_f32 v[236:237], v[12:13], s[0:1], v[236:237] op_sel_hi:[1,0,1]
	v_pk_fma_f32 v[238:239], v[14:15], s[0:1], v[238:239] op_sel_hi:[1,0,1]
	v_cvt_pk_f32_fp8_e32 v[8:9], v36
	v_cvt_pk_f32_fp8_sdwa v[10:11], v36 src0_sel:WORD_1
	v_pk_fma_f32 v[224:225], v[8:9], s[2:3], v[224:225] op_sel_hi:[1,0,1]
	v_pk_fma_f32 v[226:227], v[10:11], s[2:3], v[226:227] op_sel_hi:[1,0,1]
	v_cvt_pk_f32_fp8_e32 v[12:13], v37
	v_cvt_pk_f32_fp8_sdwa v[14:15], v37 src0_sel:WORD_1
	v_pk_fma_f32 v[228:229], v[12:13], s[2:3], v[228:229] op_sel_hi:[1,0,1]
	v_pk_fma_f32 v[230:231], v[14:15], s[2:3], v[230:231] op_sel_hi:[1,0,1]
	v_cvt_pk_f32_fp8_e32 v[8:9], v38
	v_cvt_pk_f32_fp8_sdwa v[10:11], v38 src0_sel:WORD_1
	v_pk_fma_f32 v[232:233], v[8:9], s[2:3], v[232:233] op_sel_hi:[1,0,1]
	v_pk_fma_f32 v[234:235], v[10:11], s[2:3], v[234:235] op_sel_hi:[1,0,1]
	v_cvt_pk_f32_fp8_e32 v[12:13], v39
	v_cvt_pk_f32_fp8_sdwa v[14:15], v39 src0_sel:WORD_1
	v_pk_fma_f32 v[236:237], v[12:13], s[2:3], v[236:237] op_sel_hi:[1,0,1]
	v_pk_fma_f32 v[238:239], v[14:15], s[2:3], v[238:239] op_sel_hi:[1,0,1]
	v_cvt_pk_f32_fp8_e32 v[8:9], v44
	v_cvt_pk_f32_fp8_sdwa v[10:11], v44 src0_sel:WORD_1
	v_pk_fma_f32 v[224:225], v[8:9], s[4:5], v[224:225] op_sel_hi:[1,0,1]
	v_pk_fma_f32 v[226:227], v[10:11], s[4:5], v[226:227] op_sel_hi:[1,0,1]
	v_cvt_pk_f32_fp8_e32 v[12:13], v45
	v_cvt_pk_f32_fp8_sdwa v[14:15], v45 src0_sel:WORD_1
	v_pk_fma_f32 v[228:229], v[12:13], s[4:5], v[228:229] op_sel_hi:[1,0,1]
	v_pk_fma_f32 v[230:231], v[14:15], s[4:5], v[230:231] op_sel_hi:[1,0,1]
	v_cvt_pk_f32_fp8_e32 v[8:9], v46
	v_cvt_pk_f32_fp8_sdwa v[10:11], v46 src0_sel:WORD_1
	v_pk_fma_f32 v[232:233], v[8:9], s[4:5], v[232:233] op_sel_hi:[1,0,1]
	v_pk_fma_f32 v[234:235], v[10:11], s[4:5], v[234:235] op_sel_hi:[1,0,1]
	v_cvt_pk_f32_fp8_e32 v[12:13], v47
	v_cvt_pk_f32_fp8_sdwa v[14:15], v47 src0_sel:WORD_1
	v_pk_fma_f32 v[236:237], v[12:13], s[4:5], v[236:237] op_sel_hi:[1,0,1]
	v_pk_fma_f32 v[238:239], v[14:15], s[4:5], v[238:239] op_sel_hi:[1,0,1]
	v_cvt_pk_f32_fp8_e32 v[8:9], v52
	v_cvt_pk_f32_fp8_sdwa v[10:11], v52 src0_sel:WORD_1
	v_pk_fma_f32 v[224:225], v[8:9], s[6:7], v[224:225] op_sel_hi:[1,0,1]
	v_pk_fma_f32 v[226:227], v[10:11], s[6:7], v[226:227] op_sel_hi:[1,0,1]
	v_cvt_pk_f32_fp8_e32 v[12:13], v53
	v_cvt_pk_f32_fp8_sdwa v[14:15], v53 src0_sel:WORD_1
	v_pk_fma_f32 v[228:229], v[12:13], s[6:7], v[228:229] op_sel_hi:[1,0,1]
	v_pk_fma_f32 v[230:231], v[14:15], s[6:7], v[230:231] op_sel_hi:[1,0,1]
	v_cvt_pk_f32_fp8_e32 v[8:9], v54
	v_cvt_pk_f32_fp8_sdwa v[10:11], v54 src0_sel:WORD_1
	v_pk_fma_f32 v[232:233], v[8:9], s[6:7], v[232:233] op_sel_hi:[1,0,1]
	v_pk_fma_f32 v[234:235], v[10:11], s[6:7], v[234:235] op_sel_hi:[1,0,1]
	v_cvt_pk_f32_fp8_e32 v[12:13], v55
	v_cvt_pk_f32_fp8_sdwa v[14:15], v55 src0_sel:WORD_1
	v_pk_fma_f32 v[236:237], v[12:13], s[6:7], v[236:237] op_sel_hi:[1,0,1]
	v_pk_fma_f32 v[238:239], v[14:15], s[6:7], v[238:239] op_sel_hi:[1,0,1]
	v_cvt_pk_f32_fp8_e32 v[8:9], v60
	v_cvt_pk_f32_fp8_sdwa v[10:11], v60 src0_sel:WORD_1
	v_pk_fma_f32 v[224:225], v[8:9], s[8:9], v[224:225] op_sel_hi:[1,0,1]
	v_pk_fma_f32 v[226:227], v[10:11], s[8:9], v[226:227] op_sel_hi:[1,0,1]
	v_cvt_pk_f32_fp8_e32 v[12:13], v61
	v_cvt_pk_f32_fp8_sdwa v[14:15], v61 src0_sel:WORD_1
	v_pk_fma_f32 v[228:229], v[12:13], s[8:9], v[228:229] op_sel_hi:[1,0,1]
	v_pk_fma_f32 v[230:231], v[14:15], s[8:9], v[230:231] op_sel_hi:[1,0,1]
	v_cvt_pk_f32_fp8_e32 v[8:9], v62
	v_cvt_pk_f32_fp8_sdwa v[10:11], v62 src0_sel:WORD_1
	v_pk_fma_f32 v[232:233], v[8:9], s[8:9], v[232:233] op_sel_hi:[1,0,1]
	v_pk_fma_f32 v[234:235], v[10:11], s[8:9], v[234:235] op_sel_hi:[1,0,1]
	v_cvt_pk_f32_fp8_e32 v[12:13], v63
	v_cvt_pk_f32_fp8_sdwa v[14:15], v63 src0_sel:WORD_1
	v_pk_fma_f32 v[236:237], v[12:13], s[8:9], v[236:237] op_sel_hi:[1,0,1]
	v_pk_fma_f32 v[238:239], v[14:15], s[8:9], v[238:239] op_sel_hi:[1,0,1]
	v_cvt_pk_f32_fp8_e32 v[8:9], v68
	v_cvt_pk_f32_fp8_sdwa v[10:11], v68 src0_sel:WORD_1
	v_pk_fma_f32 v[224:225], v[8:9], s[10:11], v[224:225] op_sel_hi:[1,0,1]
	v_pk_fma_f32 v[226:227], v[10:11], s[10:11], v[226:227] op_sel_hi:[1,0,1]
	v_cvt_pk_f32_fp8_e32 v[12:13], v69
	v_cvt_pk_f32_fp8_sdwa v[14:15], v69 src0_sel:WORD_1
	v_pk_fma_f32 v[228:229], v[12:13], s[10:11], v[228:229] op_sel_hi:[1,0,1]
	v_pk_fma_f32 v[230:231], v[14:15], s[10:11], v[230:231] op_sel_hi:[1,0,1]
	v_cvt_pk_f32_fp8_e32 v[8:9], v70
	v_cvt_pk_f32_fp8_sdwa v[10:11], v70 src0_sel:WORD_1
	v_pk_fma_f32 v[232:233], v[8:9], s[10:11], v[232:233] op_sel_hi:[1,0,1]
	v_pk_fma_f32 v[234:235], v[10:11], s[10:11], v[234:235] op_sel_hi:[1,0,1]
	v_cvt_pk_f32_fp8_e32 v[12:13], v71
	v_cvt_pk_f32_fp8_sdwa v[14:15], v71 src0_sel:WORD_1
	v_pk_fma_f32 v[236:237], v[12:13], s[10:11], v[236:237] op_sel_hi:[1,0,1]
	v_pk_fma_f32 v[238:239], v[14:15], s[10:11], v[238:239] op_sel_hi:[1,0,1]
	v_cvt_pk_f32_fp8_e32 v[8:9], v76
	v_cvt_pk_f32_fp8_sdwa v[10:11], v76 src0_sel:WORD_1
	v_pk_fma_f32 v[224:225], v[8:9], s[12:13], v[224:225] op_sel_hi:[1,0,1]
	v_pk_fma_f32 v[226:227], v[10:11], s[12:13], v[226:227] op_sel_hi:[1,0,1]
	v_cvt_pk_f32_fp8_e32 v[12:13], v77
	v_cvt_pk_f32_fp8_sdwa v[14:15], v77 src0_sel:WORD_1
	v_pk_fma_f32 v[228:229], v[12:13], s[12:13], v[228:229] op_sel_hi:[1,0,1]
	v_pk_fma_f32 v[230:231], v[14:15], s[12:13], v[230:231] op_sel_hi:[1,0,1]
	v_cvt_pk_f32_fp8_e32 v[8:9], v78
	v_cvt_pk_f32_fp8_sdwa v[10:11], v78 src0_sel:WORD_1
	v_pk_fma_f32 v[232:233], v[8:9], s[12:13], v[232:233] op_sel_hi:[1,0,1]
	v_pk_fma_f32 v[234:235], v[10:11], s[12:13], v[234:235] op_sel_hi:[1,0,1]
	v_cvt_pk_f32_fp8_e32 v[12:13], v79
	v_cvt_pk_f32_fp8_sdwa v[14:15], v79 src0_sel:WORD_1
	v_pk_fma_f32 v[236:237], v[12:13], s[12:13], v[236:237] op_sel_hi:[1,0,1]
	v_pk_fma_f32 v[238:239], v[14:15], s[12:13], v[238:239] op_sel_hi:[1,0,1]
	v_cvt_pk_f32_fp8_e32 v[8:9], v84
	v_cvt_pk_f32_fp8_sdwa v[10:11], v84 src0_sel:WORD_1
	v_pk_fma_f32 v[224:225], v[8:9], s[14:15], v[224:225] op_sel_hi:[1,0,1]
	v_pk_fma_f32 v[226:227], v[10:11], s[14:15], v[226:227] op_sel_hi:[1,0,1]
	v_cvt_pk_f32_fp8_e32 v[12:13], v85
	v_cvt_pk_f32_fp8_sdwa v[14:15], v85 src0_sel:WORD_1
	v_pk_fma_f32 v[228:229], v[12:13], s[14:15], v[228:229] op_sel_hi:[1,0,1]
	v_pk_fma_f32 v[230:231], v[14:15], s[14:15], v[230:231] op_sel_hi:[1,0,1]
	v_cvt_pk_f32_fp8_e32 v[8:9], v86
	v_cvt_pk_f32_fp8_sdwa v[10:11], v86 src0_sel:WORD_1
	v_pk_fma_f32 v[232:233], v[8:9], s[14:15], v[232:233] op_sel_hi:[1,0,1]
	v_pk_fma_f32 v[234:235], v[10:11], s[14:15], v[234:235] op_sel_hi:[1,0,1]
	v_cvt_pk_f32_fp8_e32 v[12:13], v87
	v_cvt_pk_f32_fp8_sdwa v[14:15], v87 src0_sel:WORD_1
	v_pk_fma_f32 v[236:237], v[12:13], s[14:15], v[236:237] op_sel_hi:[1,0,1]
	v_pk_fma_f32 v[238:239], v[14:15], s[14:15], v[238:239] op_sel_hi:[1,0,1]
	v_lshlrev_b32_e32 v240, 16, v96
	v_and_b32_e32 v241, 0xffff0000, v96
	v_lshlrev_b32_e32 v242, 16, v97
	v_and_b32_e32 v243, 0xffff0000, v97
	v_lshlrev_b32_e32 v244, 16, v98
	v_and_b32_e32 v245, 0xffff0000, v98
	v_lshlrev_b32_e32 v246, 16, v99
	v_and_b32_e32 v247, 0xffff0000, v99
	v_lshlrev_b32_e32 v248, 16, v100
	v_and_b32_e32 v249, 0xffff0000, v100
	v_lshlrev_b32_e32 v250, 16, v101
	v_and_b32_e32 v251, 0xffff0000, v101
	v_lshlrev_b32_e32 v252, 16, v102
	v_and_b32_e32 v253, 0xffff0000, v102
	v_lshlrev_b32_e32 v254, 16, v103
	v_and_b32_e32 v255, 0xffff0000, v103
	v_pk_fma_f32 v[240:241], v[224:225], v[208:209], v[240:241]
	v_pk_fma_f32 v[242:243], v[226:227], v[210:211], v[242:243]
	v_pk_fma_f32 v[244:245], v[228:229], v[212:213], v[244:245]
	v_pk_fma_f32 v[246:247], v[230:231], v[214:215], v[246:247]
	v_pk_fma_f32 v[248:249], v[232:233], v[216:217], v[248:249]
	v_pk_fma_f32 v[250:251], v[234:235], v[218:219], v[250:251]
	v_pk_fma_f32 v[252:253], v[236:237], v[220:221], v[252:253]
	v_pk_fma_f32 v[254:255], v[238:239], v[222:223], v[254:255]
	global_store_dwordx4 v2, v[240:243], s[68:69]
	global_store_dwordx4 v2, v[244:247], s[68:69] offset:16
	global_store_dwordx4 v2, v[248:251], s[68:69] offset:32
	global_store_dwordx4 v2, v[252:255], s[68:69] offset:48
	s_cmp_lt_u32 s78, 0x2000
	s_cbranch_scc0 .Lcomb_done
	s_mov_b32 s66, s78
	s_lshr_b32 s67, s66, 12
	s_mul_i32 s67, s67, 0xc000
	s_add_u32 s68, s64, s67
	s_addc_u32 s69, s65, 0
	global_load_dwordx4 v[192:195], v2, s[68:69]
	global_load_dwordx4 v[196:199], v2, s[68:69] offset:16
	global_load_dwordx4 v[200:203], v2, s[68:69] offset:32
	global_load_dwordx4 v[204:207], v2, s[68:69] offset:48
	s_add_u32 s68, s68, 0x1000
	s_addc_u32 s69, s69, 0
	global_load_dwordx4 v[208:211], v2, s[68:69]
	global_load_dwordx4 v[212:215], v2, s[68:69] offset:16
	global_load_dwordx4 v[216:219], v2, s[68:69] offset:32
	global_load_dwordx4 v[220:223], v2, s[68:69] offset:48
	s_waitcnt vmcnt(16)
	s_cmp_lt_u32 s79, 0x2000
	s_cbranch_scc0 .Lcomb_sk4
	v_lshlrev_b32_e32 v7, 2, v4
	v_add_u32_e32 v7, 0x21540, v7
	ds_read_b32 v7, v7
	s_waitcnt lgkmcnt(0)
	v_add_u32_e32 v7, v7, v5
	s_nop 1
	v_readlane_b32 s70, v7, 0
	v_readlane_b32 s71, v7, 1
	v_readlane_b32 s72, v7, 2
	v_readlane_b32 s73, v7, 3
	v_readlane_b32 s74, v7, 4
	v_readlane_b32 s75, v7, 5
	v_readlane_b32 s76, v7, 6
	v_readlane_b32 s77, v7, 7
	v_readlane_b32 s0, v6, 0
	v_readlane_b32 s2, v6, 1
	v_readlane_b32 s4, v6, 2
	v_readlane_b32 s6, v6, 3
	v_readlane_b32 s8, v6, 4
	v_readlane_b32 s10, v6, 5
	v_readlane_b32 s12, v6, 6
	v_readlane_b32 s14, v6, 7
	s_mov_b32 s66, s79
	s_lshl_b32 s67, s66, 12
	s_add_u32 s68, s62, s67
	s_addc_u32 s69, s63, 0
	global_load_dwordx4 v[88:91], v1, s[68:69] nt
	global_load_dwordx4 v[92:95], v1, s[68:69] offset:16 nt
	global_load_dwordx4 v[96:99], v1, s[68:69] offset:2048 nt
	global_load_dwordx4 v[100:103], v1, s[68:69] offset:2064 nt
	s_add_u32 s67, s66, 0x10000
	s_lshl_b32 s67, s67, 11
	s_add_u32 s68, s60, s67
	s_addc_u32 s69, s61, 0
	global_load_dwordx4 v[16:19], v0, s[68:69] nt
	global_load_dwordx4 v[20:23], v0, s[68:69] offset:1024 nt
	s_lshl_b32 s67, s70, 11
	s_add_u32 s68, s60, s67
	s_addc_u32 s69, s61, 0
	global_load_dwordx4 v[24:27], v0, s[68:69] nt
	global_load_dwordx4 v[28:31], v0, s[68:69] offset:1024 nt
	s_lshl_b32 s67, s71, 11
	s_add_u32 s68, s60, s67
	s_addc_u32 s69, s61, 0
	global_load_dwordx4 v[32:35], v0, s[68:69] nt
	global_load_dwordx4 v[36:39], v0, s[68:69] offset:1024 nt
	s_lshl_b32 s67, s72, 11
	s_add_u32 s68, s60, s67
	s_addc_u32 s69, s61, 0
	global_load_dwordx4 v[40:43], v0, s[68:69] nt
	global_load_dwordx4 v[44:47], v0, s[68:69] offset:1024 nt
	s_lshl_b32 s67, s73, 11
	s_add_u32 s68, s60, s67
	s_addc_u32 s69, s61, 0
	global_load_dwordx4 v[48:51], v0, s[68:69] nt
	global_load_dwordx4 v[52:55], v0, s[68:69] offset:1024 nt
	s_lshl_b32 s67, s74, 11
	s_add_u32 s68, s60, s67
	s_addc_u32 s69, s61, 0
	global_load_dwordx4 v[56:59], v0, s[68:69] nt
	global_load_dwordx4 v[60:63], v0, s[68:69] offset:1024 nt
	s_lshl_b32 s67, s75, 11
	s_add_u32 s68, s60, s67
	s_addc_u32 s69, s61, 0
	global_load_dwordx4 v[64:67], v0, s[68:69] nt
	global_load_dwordx4 v[68:71], v0, s[68:69] offset:1024 nt
	s_lshl_b32 s67, s76, 11
	s_add_u32 s68, s60, s67
	s_addc_u32 s69, s61, 0
	global_load_dwordx4 v[72:75], v0, s[68:69] nt
	global_load_dwordx4 v[76:79], v0, s[68:69] offset:1024 nt
	s_lshl_b32 s67, s77, 11
	s_add_u32 s68, s60, s67
	s_addc_u32 s69, s61, 0
	global_load_dwordx4 v[80:83], v0, s[68:69] nt
	global_load_dwordx4 v[84:87], v0, s[68:69] offset:1024 nt
.Lcomb_sk4:
	s_add_u32 s52, s79, s53
	s_cmp_lt_u32 s52, 0x2000
	s_cbranch_scc0 .Lcomb_sk5
	s_mov_b32 s66, s52
	s_lshl_b32 s66, s66, 5
	s_add_u32 s68, s54, s66
	s_addc_u32 s69, s55, 0
	global_load_dword v4, v3, s[68:69]
	s_add_u32 s68, s56, s66
	s_addc_u32 s69, s57, 0
	global_load_dword v5, v3, s[68:69]
	s_add_u32 s68, s58, s66
	s_addc_u32 s69, s59, 0
	global_load_dword v6, v3, s[68:69]
.Lcomb_sk5:
	s_lshl_b32 s67, s78, 13
	s_add_u32 s68, s48, s67
	s_addc_u32 s69, s49, 0
	v_cvt_pk_f32_fp8_e32 v[224:225], v104
	v_cvt_pk_f32_fp8_sdwa v[226:227], v104 src0_sel:WORD_1
	v_cvt_pk_f32_fp8_e32 v[228:229], v105
	v_cvt_pk_f32_fp8_sdwa v[230:231], v105 src0_sel:WORD_1
	v_cvt_pk_f32_fp8_e32 v[232:233], v106
	v_cvt_pk_f32_fp8_sdwa v[234:235], v106 src0_sel:WORD_1
	v_cvt_pk_f32_fp8_e32 v[236:237], v107
	v_cvt_pk_f32_fp8_sdwa v[238:239], v107 src0_sel:WORD_1
	v_cvt_pk_f32_fp8_e32 v[8:9], v112
	v_cvt_pk_f32_fp8_sdwa v[10:11], v112 src0_sel:WORD_1
	v_pk_fma_f32 v[224:225], v[8:9], s[16:17], v[224:225] op_sel_hi:[1,0,1]
	v_pk_fma_f32 v[226:227], v[10:11], s[16:17], v[226:227] op_sel_hi:[1,0,1]
	v_cvt_pk_f32_fp8_e32 v[12:13], v113
	v_cvt_pk_f32_fp8_sdwa v[14:15], v113 src0_sel:WORD_1
	v_pk_fma_f32 v[228:229], v[12:13], s[16:17], v[228:229] op_sel_hi:[1,0,1]
	v_pk_fma_f32 v[230:231], v[14:15], s[16:17], v[230:231] op_sel_hi:[1,0,1]
	v_cvt_pk_f32_fp8_e32 v[8:9], v114
	v_cvt_pk_f32_fp8_sdwa v[10:11], v114 src0_sel:WORD_1
	v_pk_fma_f32 v[232:233], v[8:9], s[16:17], v[232:233] op_sel_hi:[1,0,1]
	v_pk_fma_f32 v[234:235], v[10:11], s[16:17], v[234:235] op_sel_hi:[1,0,1]
	v_cvt_pk_f32_fp8_e32 v[12:13], v115
	v_cvt_pk_f32_fp8_sdwa v[14:15], v115 src0_sel:WORD_1
	v_pk_fma_f32 v[236:237], v[12:13], s[16:17], v[236:237] op_sel_hi:[1,0,1]
	v_pk_fma_f32 v[238:239], v[14:15], s[16:17], v[238:239] op_sel_hi:[1,0,1]
	v_cvt_pk_f32_fp8_e32 v[8:9], v120
	v_cvt_pk_f32_fp8_sdwa v[10:11], v120 src0_sel:WORD_1
	v_pk_fma_f32 v[224:225], v[8:9], s[18:19], v[224:225] op_sel_hi:[1,0,1]
	v_pk_fma_f32 v[226:227], v[10:11], s[18:19], v[226:227] op_sel_hi:[1,0,1]
	v_cvt_pk_f32_fp8_e32 v[12:13], v121
	v_cvt_pk_f32_fp8_sdwa v[14:15], v121 src0_sel:WORD_1
	v_pk_fma_f32 v[228:229], v[12:13], s[18:19], v[228:229] op_sel_hi:[1,0,1]
	v_pk_fma_f32 v[230:231], v[14:15], s[18:19], v[230:231] op_sel_hi:[1,0,1]
	v_cvt_pk_f32_fp8_e32 v[8:9], v122
	v_cvt_pk_f32_fp8_sdwa v[10:11], v122 src0_sel:WORD_1
	v_pk_fma_f32 v[232:233], v[8:9], s[18:19], v[232:233] op_sel_hi:[1,0,1]
	v_pk_fma_f32 v[234:235], v[10:11], s[18:19], v[234:235] op_sel_hi:[1,0,1]
	v_cvt_pk_f32_fp8_e32 v[12:13], v123
	v_cvt_pk_f32_fp8_sdwa v[14:15], v123 src0_sel:WORD_1
	v_pk_fma_f32 v[236:237], v[12:13], s[18:19], v[236:237] op_sel_hi:[1,0,1]
	v_pk_fma_f32 v[238:239], v[14:15], s[18:19], v[238:239] op_sel_hi:[1,0,1]
	v_cvt_pk_f32_fp8_e32 v[8:9], v128
	v_cvt_pk_f32_fp8_sdwa v[10:11], v128 src0_sel:WORD_1
	v_pk_fma_f32 v[224:225], v[8:9], s[20:21], v[224:225] op_sel_hi:[1,0,1]
	v_pk_fma_f32 v[226:227], v[10:11], s[20:21], v[226:227] op_sel_hi:[1,0,1]
	v_cvt_pk_f32_fp8_e32 v[12:13], v129
	v_cvt_pk_f32_fp8_sdwa v[14:15], v129 src0_sel:WORD_1
	v_pk_fma_f32 v[228:229], v[12:13], s[20:21], v[228:229] op_sel_hi:[1,0,1]
	v_pk_fma_f32 v[230:231], v[14:15], s[20:21], v[230:231] op_sel_hi:[1,0,1]
	v_cvt_pk_f32_fp8_e32 v[8:9], v130
	v_cvt_pk_f32_fp8_sdwa v[10:11], v130 src0_sel:WORD_1
	v_pk_fma_f32 v[232:233], v[8:9], s[20:21], v[232:233] op_sel_hi:[1,0,1]
	v_pk_fma_f32 v[234:235], v[10:11], s[20:21], v[234:235] op_sel_hi:[1,0,1]
	v_cvt_pk_f32_fp8_e32 v[12:13], v131
	v_cvt_pk_f32_fp8_sdwa v[14:15], v131 src0_sel:WORD_1
	v_pk_fma_f32 v[236:237], v[12:13], s[20:21], v[236:237] op_sel_hi:[1,0,1]
	v_pk_fma_f32 v[238:239], v[14:15], s[20:21], v[238:239] op_sel_hi:[1,0,1]
	v_cvt_pk_f32_fp8_e32 v[8:9], v136
	v_cvt_pk_f32_fp8_sdwa v[10:11], v136 src0_sel:WORD_1
	v_pk_fma_f32 v[224:225], v[8:9], s[22:23], v[224:225] op_sel_hi:[1,0,1]
	v_pk_fma_f32 v[226:227], v[10:11], s[22:23], v[226:227] op_sel_hi:[1,0,1]
	v_cvt_pk_f32_fp8_e32 v[12:13], v137
	v_cvt_pk_f32_fp8_sdwa v[14:15], v137 src0_sel:WORD_1
	v_pk_fma_f32 v[228:229], v[12:13], s[22:23], v[228:229] op_sel_hi:[1,0,1]
	v_pk_fma_f32 v[230:231], v[14:15], s[22:23], v[230:231] op_sel_hi:[1,0,1]
	v_cvt_pk_f32_fp8_e32 v[8:9], v138
	v_cvt_pk_f32_fp8_sdwa v[10:11], v138 src0_sel:WORD_1
	v_pk_fma_f32 v[232:233], v[8:9], s[22:23], v[232:233] op_sel_hi:[1,0,1]
	v_pk_fma_f32 v[234:235], v[10:11], s[22:23], v[234:235] op_sel_hi:[1,0,1]
	v_cvt_pk_f32_fp8_e32 v[12:13], v139
	v_cvt_pk_f32_fp8_sdwa v[14:15], v139 src0_sel:WORD_1
	v_pk_fma_f32 v[236:237], v[12:13], s[22:23], v[236:237] op_sel_hi:[1,0,1]
	v_pk_fma_f32 v[238:239], v[14:15], s[22:23], v[238:239] op_sel_hi:[1,0,1]
	v_cvt_pk_f32_fp8_e32 v[8:9], v144
	v_cvt_pk_f32_fp8_sdwa v[10:11], v144 src0_sel:WORD_1
	v_pk_fma_f32 v[224:225], v[8:9], s[24:25], v[224:225] op_sel_hi:[1,0,1]
	v_pk_fma_f32 v[226:227], v[10:11], s[24:25], v[226:227] op_sel_hi:[1,0,1]
	v_cvt_pk_f32_fp8_e32 v[12:13], v145
	v_cvt_pk_f32_fp8_sdwa v[14:15], v145 src0_sel:WORD_1
	v_pk_fma_f32 v[228:229], v[12:13], s[24:25], v[228:229] op_sel_hi:[1,0,1]
	v_pk_fma_f32 v[230:231], v[14:15], s[24:25], v[230:231] op_sel_hi:[1,0,1]
	v_cvt_pk_f32_fp8_e32 v[8:9], v146
	v_cvt_pk_f32_fp8_sdwa v[10:11], v146 src0_sel:WORD_1
	v_pk_fma_f32 v[232:233], v[8:9], s[24:25], v[232:233] op_sel_hi:[1,0,1]
	v_pk_fma_f32 v[234:235], v[10:11], s[24:25], v[234:235] op_sel_hi:[1,0,1]
	v_cvt_pk_f32_fp8_e32 v[12:13], v147
	v_cvt_pk_f32_fp8_sdwa v[14:15], v147 src0_sel:WORD_1
	v_pk_fma_f32 v[236:237], v[12:13], s[24:25], v[236:237] op_sel_hi:[1,0,1]
	v_pk_fma_f32 v[238:239], v[14:15], s[24:25], v[238:239] op_sel_hi:[1,0,1]
	v_cvt_pk_f32_fp8_e32 v[8:9], v152
	v_cvt_pk_f32_fp8_sdwa v[10:11], v152 src0_sel:WORD_1
	v_pk_fma_f32 v[224:225], v[8:9], s[26:27], v[224:225] op_sel_hi:[1,0,1]
	v_pk_fma_f32 v[226:227], v[10:11], s[26:27], v[226:227] op_sel_hi:[1,0,1]
	v_cvt_pk_f32_fp8_e32 v[12:13], v153
	v_cvt_pk_f32_fp8_sdwa v[14:15], v153 src0_sel:WORD_1
	v_pk_fma_f32 v[228:229], v[12:13], s[26:27], v[228:229] op_sel_hi:[1,0,1]
	v_pk_fma_f32 v[230:231], v[14:15], s[26:27], v[230:231] op_sel_hi:[1,0,1]
	v_cvt_pk_f32_fp8_e32 v[8:9], v154
	v_cvt_pk_f32_fp8_sdwa v[10:11], v154 src0_sel:WORD_1
	v_pk_fma_f32 v[232:233], v[8:9], s[26:27], v[232:233] op_sel_hi:[1,0,1]
	v_pk_fma_f32 v[234:235], v[10:11], s[26:27], v[234:235] op_sel_hi:[1,0,1]
	v_cvt_pk_f32_fp8_e32 v[12:13], v155
	v_cvt_pk_f32_fp8_sdwa v[14:15], v155 src0_sel:WORD_1
	v_pk_fma_f32 v[236:237], v[12:13], s[26:27], v[236:237] op_sel_hi:[1,0,1]
	v_pk_fma_f32 v[238:239], v[14:15], s[26:27], v[238:239] op_sel_hi:[1,0,1]
	v_cvt_pk_f32_fp8_e32 v[8:9], v160
	v_cvt_pk_f32_fp8_sdwa v[10:11], v160 src0_sel:WORD_1
	v_pk_fma_f32 v[224:225], v[8:9], s[28:29], v[224:225] op_sel_hi:[1,0,1]
	v_pk_fma_f32 v[226:227], v[10:11], s[28:29], v[226:227] op_sel_hi:[1,0,1]
	v_cvt_pk_f32_fp8_e32 v[12:13], v161
	v_cvt_pk_f32_fp8_sdwa v[14:15], v161 src0_sel:WORD_1
	v_pk_fma_f32 v[228:229], v[12:13], s[28:29], v[228:229] op_sel_hi:[1,0,1]
	v_pk_fma_f32 v[230:231], v[14:15], s[28:29], v[230:231] op_sel_hi:[1,0,1]
	v_cvt_pk_f32_fp8_e32 v[8:9], v162
	v_cvt_pk_f32_fp8_sdwa v[10:11], v162 src0_sel:WORD_1
	v_pk_fma_f32 v[232:233], v[8:9], s[28:29], v[232:233] op_sel_hi:[1,0,1]
	v_pk_fma_f32 v[234:235], v[10:11], s[28:29], v[234:235] op_sel_hi:[1,0,1]
	v_cvt_pk_f32_fp8_e32 v[12:13], v163
	v_cvt_pk_f32_fp8_sdwa v[14:15], v163 src0_sel:WORD_1
	v_pk_fma_f32 v[236:237], v[12:13], s[28:29], v[236:237] op_sel_hi:[1,0,1]
	v_pk_fma_f32 v[238:239], v[14:15], s[28:29], v[238:239] op_sel_hi:[1,0,1]
	v_cvt_pk_f32_fp8_e32 v[8:9], v168
	v_cvt_pk_f32_fp8_sdwa v[10:11], v168 src0_sel:WORD_1
	v_pk_fma_f32 v[224:225], v[8:9], s[30:31], v[224:225] op_sel_hi:[1,0,1]
	v_pk_fma_f32 v[226:227], v[10:11], s[30:31], v[226:227] op_sel_hi:[1,0,1]
	v_cvt_pk_f32_fp8_e32 v[12:13], v169
	v_cvt_pk_f32_fp8_sdwa v[14:15], v169 src0_sel:WORD_1
	v_pk_fma_f32 v[228:229], v[12:13], s[30:31], v[228:229] op_sel_hi:[1,0,1]
	v_pk_fma_f32 v[230:231], v[14:15], s[30:31], v[230:231] op_sel_hi:[1,0,1]
	v_cvt_pk_f32_fp8_e32 v[8:9], v170
	v_cvt_pk_f32_fp8_sdwa v[10:11], v170 src0_sel:WORD_1
	v_pk_fma_f32 v[232:233], v[8:9], s[30:31], v[232:233] op_sel_hi:[1,0,1]
	v_pk_fma_f32 v[234:235], v[10:11], s[30:31], v[234:235] op_sel_hi:[1,0,1]
	v_cvt_pk_f32_fp8_e32 v[12:13], v171
	v_cvt_pk_f32_fp8_sdwa v[14:15], v171 src0_sel:WORD_1
	v_pk_fma_f32 v[236:237], v[12:13], s[30:31], v[236:237] op_sel_hi:[1,0,1]
	v_pk_fma_f32 v[238:239], v[14:15], s[30:31], v[238:239] op_sel_hi:[1,0,1]
	v_lshlrev_b32_e32 v240, 16, v176
	v_and_b32_e32 v241, 0xffff0000, v176
	v_lshlrev_b32_e32 v242, 16, v177
	v_and_b32_e32 v243, 0xffff0000, v177
	v_lshlrev_b32_e32 v244, 16, v178
	v_and_b32_e32 v245, 0xffff0000, v178
	v_lshlrev_b32_e32 v246, 16, v179
	v_and_b32_e32 v247, 0xffff0000, v179
	v_lshlrev_b32_e32 v248, 16, v180
	v_and_b32_e32 v249, 0xffff0000, v180
	v_lshlrev_b32_e32 v250, 16, v181
	v_and_b32_e32 v251, 0xffff0000, v181
	v_lshlrev_b32_e32 v252, 16, v182
	v_and_b32_e32 v253, 0xffff0000, v182
	v_lshlrev_b32_e32 v254, 16, v183
	v_and_b32_e32 v255, 0xffff0000, v183
	s_cmp_lt_u32 s52, 0x2000
	s_cbranch_scc0 .Lcomb_wa6
	s_waitcnt vmcnt(25)
	s_branch .Lcomb_wj6
.Lcomb_wa6:
	s_cmp_lt_u32 s79, 0x2000
	s_cbranch_scc0 .Lcomb_wb6
	s_waitcnt vmcnt(22)
	s_branch .Lcomb_wj6

.Lcomb_wj6:
	v_pk_fma_f32 v[240:241], v[224:225], v[192:193], v[240:241]
	v_pk_fma_f32 v[242:243], v[226:227], v[194:195], v[242:243]
	v_pk_fma_f32 v[244:245], v[228:229], v[196:197], v[244:245]
	v_pk_fma_f32 v[246:247], v[230:231], v[198:199], v[246:247]
	v_pk_fma_f32 v[248:249], v[232:233], v[200:201], v[248:249]
	v_pk_fma_f32 v[250:251], v[234:235], v[202:203], v[250:251]
	v_pk_fma_f32 v[252:253], v[236:237], v[204:205], v[252:253]
	v_pk_fma_f32 v[254:255], v[238:239], v[206:207], v[254:255]
	global_store_dwordx4 v2, v[240:243], s[68:69]
	global_store_dwordx4 v2, v[244:247], s[68:69] offset:16
	global_store_dwordx4 v2, v[248:251], s[68:69] offset:32
	global_store_dwordx4 v2, v[252:255], s[68:69] offset:48
	s_add_u32 s68, s68, 0x1000
	s_addc_u32 s69, s69, 0
	v_cvt_pk_f32_fp8_e32 v[224:225], v108
	v_cvt_pk_f32_fp8_sdwa v[226:227], v108 src0_sel:WORD_1
	v_cvt_pk_f32_fp8_e32 v[228:229], v109
	v_cvt_pk_f32_fp8_sdwa v[230:231], v109 src0_sel:WORD_1
	v_cvt_pk_f32_fp8_e32 v[232:233], v110
	v_cvt_pk_f32_fp8_sdwa v[234:235], v110 src0_sel:WORD_1
	v_cvt_pk_f32_fp8_e32 v[236:237], v111
	v_cvt_pk_f32_fp8_sdwa v[238:239], v111 src0_sel:WORD_1
	v_cvt_pk_f32_fp8_e32 v[8:9], v116
	v_cvt_pk_f32_fp8_sdwa v[10:11], v116 src0_sel:WORD_1
	v_pk_fma_f32 v[224:225], v[8:9], s[16:17], v[224:225] op_sel_hi:[1,0,1]
	v_pk_fma_f32 v[226:227], v[10:11], s[16:17], v[226:227] op_sel_hi:[1,0,1]
	v_cvt_pk_f32_fp8_e32 v[12:13], v117
	v_cvt_pk_f32_fp8_sdwa v[14:15], v117 src0_sel:WORD_1
	v_pk_fma_f32 v[228:229], v[12:13], s[16:17], v[228:229] op_sel_hi:[1,0,1]
	v_pk_fma_f32 v[230:231], v[14:15], s[16:17], v[230:231] op_sel_hi:[1,0,1]
	v_cvt_pk_f32_fp8_e32 v[8:9], v118
	v_cvt_pk_f32_fp8_sdwa v[10:11], v118 src0_sel:WORD_1
	v_pk_fma_f32 v[232:233], v[8:9], s[16:17], v[232:233] op_sel_hi:[1,0,1]
	v_pk_fma_f32 v[234:235], v[10:11], s[16:17], v[234:235] op_sel_hi:[1,0,1]
	v_cvt_pk_f32_fp8_e32 v[12:13], v119
	v_cvt_pk_f32_fp8_sdwa v[14:15], v119 src0_sel:WORD_1
	v_pk_fma_f32 v[236:237], v[12:13], s[16:17], v[236:237] op_sel_hi:[1,0,1]
	v_pk_fma_f32 v[238:239], v[14:15], s[16:17], v[238:239] op_sel_hi:[1,0,1]
	v_cvt_pk_f32_fp8_e32 v[8:9], v124
	v_cvt_pk_f32_fp8_sdwa v[10:11], v124 src0_sel:WORD_1
	v_pk_fma_f32 v[224:225], v[8:9], s[18:19], v[224:225] op_sel_hi:[1,0,1]
	v_pk_fma_f32 v[226:227], v[10:11], s[18:19], v[226:227] op_sel_hi:[1,0,1]
	v_cvt_pk_f32_fp8_e32 v[12:13], v125
	v_cvt_pk_f32_fp8_sdwa v[14:15], v125 src0_sel:WORD_1
	v_pk_fma_f32 v[228:229], v[12:13], s[18:19], v[228:229] op_sel_hi:[1,0,1]
	v_pk_fma_f32 v[230:231], v[14:15], s[18:19], v[230:231] op_sel_hi:[1,0,1]
	v_cvt_pk_f32_fp8_e32 v[8:9], v126
	v_cvt_pk_f32_fp8_sdwa v[10:11], v126 src0_sel:WORD_1
	v_pk_fma_f32 v[232:233], v[8:9], s[18:19], v[232:233] op_sel_hi:[1,0,1]
	v_pk_fma_f32 v[234:235], v[10:11], s[18:19], v[234:235] op_sel_hi:[1,0,1]
	v_cvt_pk_f32_fp8_e32 v[12:13], v127
	v_cvt_pk_f32_fp8_sdwa v[14:15], v127 src0_sel:WORD_1
	v_pk_fma_f32 v[236:237], v[12:13], s[18:19], v[236:237] op_sel_hi:[1,0,1]
	v_pk_fma_f32 v[238:239], v[14:15], s[18:19], v[238:239] op_sel_hi:[1,0,1]
	v_cvt_pk_f32_fp8_e32 v[8:9], v132
	v_cvt_pk_f32_fp8_sdwa v[10:11], v132 src0_sel:WORD_1
	v_pk_fma_f32 v[224:225], v[8:9], s[20:21], v[224:225] op_sel_hi:[1,0,1]
	v_pk_fma_f32 v[226:227], v[10:11], s[20:21], v[226:227] op_sel_hi:[1,0,1]
	v_cvt_pk_f32_fp8_e32 v[12:13], v133
	v_cvt_pk_f32_fp8_sdwa v[14:15], v133 src0_sel:WORD_1
	v_pk_fma_f32 v[228:229], v[12:13], s[20:21], v[228:229] op_sel_hi:[1,0,1]
	v_pk_fma_f32 v[230:231], v[14:15], s[20:21], v[230:231] op_sel_hi:[1,0,1]
	v_cvt_pk_f32_fp8_e32 v[8:9], v134
	v_cvt_pk_f32_fp8_sdwa v[10:11], v134 src0_sel:WORD_1
	v_pk_fma_f32 v[232:233], v[8:9], s[20:21], v[232:233] op_sel_hi:[1,0,1]
	v_pk_fma_f32 v[234:235], v[10:11], s[20:21], v[234:235] op_sel_hi:[1,0,1]
	v_cvt_pk_f32_fp8_e32 v[12:13], v135
	v_cvt_pk_f32_fp8_sdwa v[14:15], v135 src0_sel:WORD_1
	v_pk_fma_f32 v[236:237], v[12:13], s[20:21], v[236:237] op_sel_hi:[1,0,1]
	v_pk_fma_f32 v[238:239], v[14:15], s[20:21], v[238:239] op_sel_hi:[1,0,1]
	v_cvt_pk_f32_fp8_e32 v[8:9], v140
	v_cvt_pk_f32_fp8_sdwa v[10:11], v140 src0_sel:WORD_1
	v_pk_fma_f32 v[224:225], v[8:9], s[22:23], v[224:225] op_sel_hi:[1,0,1]
	v_pk_fma_f32 v[226:227], v[10:11], s[22:23], v[226:227] op_sel_hi:[1,0,1]
	v_cvt_pk_f32_fp8_e32 v[12:13], v141
	v_cvt_pk_f32_fp8_sdwa v[14:15], v141 src0_sel:WORD_1
	v_pk_fma_f32 v[228:229], v[12:13], s[22:23], v[228:229] op_sel_hi:[1,0,1]
	v_pk_fma_f32 v[230:231], v[14:15], s[22:23], v[230:231] op_sel_hi:[1,0,1]
	v_cvt_pk_f32_fp8_e32 v[8:9], v142
	v_cvt_pk_f32_fp8_sdwa v[10:11], v142 src0_sel:WORD_1
	v_pk_fma_f32 v[232:233], v[8:9], s[22:23], v[232:233] op_sel_hi:[1,0,1]
	v_pk_fma_f32 v[234:235], v[10:11], s[22:23], v[234:235] op_sel_hi:[1,0,1]
	v_cvt_pk_f32_fp8_e32 v[12:13], v143
	v_cvt_pk_f32_fp8_sdwa v[14:15], v143 src0_sel:WORD_1
	v_pk_fma_f32 v[236:237], v[12:13], s[22:23], v[236:237] op_sel_hi:[1,0,1]
	v_pk_fma_f32 v[238:239], v[14:15], s[22:23], v[238:239] op_sel_hi:[1,0,1]
	v_cvt_pk_f32_fp8_e32 v[8:9], v148
	v_cvt_pk_f32_fp8_sdwa v[10:11], v148 src0_sel:WORD_1
	v_pk_fma_f32 v[224:225], v[8:9], s[24:25], v[224:225] op_sel_hi:[1,0,1]
	v_pk_fma_f32 v[226:227], v[10:11], s[24:25], v[226:227] op_sel_hi:[1,0,1]
	v_cvt_pk_f32_fp8_e32 v[12:13], v149
	v_cvt_pk_f32_fp8_sdwa v[14:15], v149 src0_sel:WORD_1
	v_pk_fma_f32 v[228:229], v[12:13], s[24:25], v[228:229] op_sel_hi:[1,0,1]
	v_pk_fma_f32 v[230:231], v[14:15], s[24:25], v[230:231] op_sel_hi:[1,0,1]
	v_cvt_pk_f32_fp8_e32 v[8:9], v150
	v_cvt_pk_f32_fp8_sdwa v[10:11], v150 src0_sel:WORD_1
	v_pk_fma_f32 v[232:233], v[8:9], s[24:25], v[232:233] op_sel_hi:[1,0,1]
	v_pk_fma_f32 v[234:235], v[10:11], s[24:25], v[234:235] op_sel_hi:[1,0,1]
	v_cvt_pk_f32_fp8_e32 v[12:13], v151
	v_cvt_pk_f32_fp8_sdwa v[14:15], v151 src0_sel:WORD_1
	v_pk_fma_f32 v[236:237], v[12:13], s[24:25], v[236:237] op_sel_hi:[1,0,1]
	v_pk_fma_f32 v[238:239], v[14:15], s[24:25], v[238:239] op_sel_hi:[1,0,1]
	v_cvt_pk_f32_fp8_e32 v[8:9], v156
	v_cvt_pk_f32_fp8_sdwa v[10:11], v156 src0_sel:WORD_1
	v_pk_fma_f32 v[224:225], v[8:9], s[26:27], v[224:225] op_sel_hi:[1,0,1]
	v_pk_fma_f32 v[226:227], v[10:11], s[26:27], v[226:227] op_sel_hi:[1,0,1]
	v_cvt_pk_f32_fp8_e32 v[12:13], v157
	v_cvt_pk_f32_fp8_sdwa v[14:15], v157 src0_sel:WORD_1
	v_pk_fma_f32 v[228:229], v[12:13], s[26:27], v[228:229] op_sel_hi:[1,0,1]
	v_pk_fma_f32 v[230:231], v[14:15], s[26:27], v[230:231] op_sel_hi:[1,0,1]
	v_cvt_pk_f32_fp8_e32 v[8:9], v158
	v_cvt_pk_f32_fp8_sdwa v[10:11], v158 src0_sel:WORD_1
	v_pk_fma_f32 v[232:233], v[8:9], s[26:27], v[232:233] op_sel_hi:[1,0,1]
	v_pk_fma_f32 v[234:235], v[10:11], s[26:27], v[234:235] op_sel_hi:[1,0,1]
	v_cvt_pk_f32_fp8_e32 v[12:13], v159
	v_cvt_pk_f32_fp8_sdwa v[14:15], v159 src0_sel:WORD_1
	v_pk_fma_f32 v[236:237], v[12:13], s[26:27], v[236:237] op_sel_hi:[1,0,1]
	v_pk_fma_f32 v[238:239], v[14:15], s[26:27], v[238:239] op_sel_hi:[1,0,1]
	v_cvt_pk_f32_fp8_e32 v[8:9], v164
	v_cvt_pk_f32_fp8_sdwa v[10:11], v164 src0_sel:WORD_1
	v_pk_fma_f32 v[224:225], v[8:9], s[28:29], v[224:225] op_sel_hi:[1,0,1]
	v_pk_fma_f32 v[226:227], v[10:11], s[28:29], v[226:227] op_sel_hi:[1,0,1]
	v_cvt_pk_f32_fp8_e32 v[12:13], v165
	v_cvt_pk_f32_fp8_sdwa v[14:15], v165 src0_sel:WORD_1
	v_pk_fma_f32 v[228:229], v[12:13], s[28:29], v[228:229] op_sel_hi:[1,0,1]
	v_pk_fma_f32 v[230:231], v[14:15], s[28:29], v[230:231] op_sel_hi:[1,0,1]
	v_cvt_pk_f32_fp8_e32 v[8:9], v166
	v_cvt_pk_f32_fp8_sdwa v[10:11], v166 src0_sel:WORD_1
	v_pk_fma_f32 v[232:233], v[8:9], s[28:29], v[232:233] op_sel_hi:[1,0,1]
	v_pk_fma_f32 v[234:235], v[10:11], s[28:29], v[234:235] op_sel_hi:[1,0,1]
	v_cvt_pk_f32_fp8_e32 v[12:13], v167
	v_cvt_pk_f32_fp8_sdwa v[14:15], v167 src0_sel:WORD_1
	v_pk_fma_f32 v[236:237], v[12:13], s[28:29], v[236:237] op_sel_hi:[1,0,1]
	v_pk_fma_f32 v[238:239], v[14:15], s[28:29], v[238:239] op_sel_hi:[1,0,1]
	v_cvt_pk_f32_fp8_e32 v[8:9], v172
	v_cvt_pk_f32_fp8_sdwa v[10:11], v172 src0_sel:WORD_1
	v_pk_fma_f32 v[224:225], v[8:9], s[30:31], v[224:225] op_sel_hi:[1,0,1]
	v_pk_fma_f32 v[226:227], v[10:11], s[30:31], v[226:227] op_sel_hi:[1,0,1]
	v_cvt_pk_f32_fp8_e32 v[12:13], v173
	v_cvt_pk_f32_fp8_sdwa v[14:15], v173 src0_sel:WORD_1
	v_pk_fma_f32 v[228:229], v[12:13], s[30:31], v[228:229] op_sel_hi:[1,0,1]
	v_pk_fma_f32 v[230:231], v[14:15], s[30:31], v[230:231] op_sel_hi:[1,0,1]
	v_cvt_pk_f32_fp8_e32 v[8:9], v174
	v_cvt_pk_f32_fp8_sdwa v[10:11], v174 src0_sel:WORD_1
	v_pk_fma_f32 v[232:233], v[8:9], s[30:31], v[232:233] op_sel_hi:[1,0,1]
	v_pk_fma_f32 v[234:235], v[10:11], s[30:31], v[234:235] op_sel_hi:[1,0,1]
	v_cvt_pk_f32_fp8_e32 v[12:13], v175
	v_cvt_pk_f32_fp8_sdwa v[14:15], v175 src0_sel:WORD_1
	v_pk_fma_f32 v[236:237], v[12:13], s[30:31], v[236:237] op_sel_hi:[1,0,1]
	v_pk_fma_f32 v[238:239], v[14:15], s[30:31], v[238:239] op_sel_hi:[1,0,1]
	v_lshlrev_b32_e32 v240, 16, v184
	v_and_b32_e32 v241, 0xffff0000, v184
	v_lshlrev_b32_e32 v242, 16, v185
	v_and_b32_e32 v243, 0xffff0000, v185
	v_lshlrev_b32_e32 v244, 16, v186
	v_and_b32_e32 v245, 0xffff0000, v186
	v_lshlrev_b32_e32 v246, 16, v187
	v_and_b32_e32 v247, 0xffff0000, v187
	v_lshlrev_b32_e32 v248, 16, v188
	v_and_b32_e32 v249, 0xffff0000, v188
	v_lshlrev_b32_e32 v250, 16, v189
	v_and_b32_e32 v251, 0xffff0000, v189
	v_lshlrev_b32_e32 v252, 16, v190
	v_and_b32_e32 v253, 0xffff0000, v190
	v_lshlrev_b32_e32 v254, 16, v191
	v_and_b32_e32 v255, 0xffff0000, v191
	v_pk_fma_f32 v[240:241], v[224:225], v[208:209], v[240:241]
	v_pk_fma_f32 v[242:243], v[226:227], v[210:211], v[242:243]
	v_pk_fma_f32 v[244:245], v[228:229], v[212:213], v[244:245]
	v_pk_fma_f32 v[246:247], v[230:231], v[214:215], v[246:247]
	v_pk_fma_f32 v[248:249], v[232:233], v[216:217], v[248:249]
	v_pk_fma_f32 v[250:251], v[234:235], v[218:219], v[250:251]
	v_pk_fma_f32 v[252:253], v[236:237], v[220:221], v[252:253]
	v_pk_fma_f32 v[254:255], v[238:239], v[222:223], v[254:255]
	global_store_dwordx4 v2, v[240:243], s[68:69]
	global_store_dwordx4 v2, v[244:247], s[68:69] offset:16
	global_store_dwordx4 v2, v[248:251], s[68:69] offset:32
	global_store_dwordx4 v2, v[252:255], s[68:69] offset:48
	s_cmp_lt_u32 s79, 0x2000
	s_cbranch_scc0 .Lcomb_done
	s_mov_b32 s66, s79
	s_lshr_b32 s67, s66, 12
	s_mul_i32 s67, s67, 0xc000
	s_add_u32 s68, s64, s67
	s_addc_u32 s69, s65, 0
	global_load_dwordx4 v[192:195], v2, s[68:69]
	global_load_dwordx4 v[196:199], v2, s[68:69] offset:16
	global_load_dwordx4 v[200:203], v2, s[68:69] offset:32
	global_load_dwordx4 v[204:207], v2, s[68:69] offset:48
	s_add_u32 s68, s68, 0x1000
	s_addc_u32 s69, s69, 0
	global_load_dwordx4 v[208:211], v2, s[68:69]
	global_load_dwordx4 v[212:215], v2, s[68:69] offset:16
	global_load_dwordx4 v[216:219], v2, s[68:69] offset:32
	global_load_dwordx4 v[220:223], v2, s[68:69] offset:48
	s_waitcnt vmcnt(16)
	s_cmp_lt_u32 s52, 0x2000
	s_cbranch_scc0 .Lcomb_sk7
	v_lshlrev_b32_e32 v7, 2, v4
	v_add_u32_e32 v7, 0x21540, v7
	ds_read_b32 v7, v7
	s_waitcnt lgkmcnt(0)
	v_add_u32_e32 v7, v7, v5
	s_nop 1
	v_readlane_b32 s70, v7, 0
	v_readlane_b32 s71, v7, 1
	v_readlane_b32 s72, v7, 2
	v_readlane_b32 s73, v7, 3
	v_readlane_b32 s74, v7, 4
	v_readlane_b32 s75, v7, 5
	v_readlane_b32 s76, v7, 6
	v_readlane_b32 s77, v7, 7
	v_readlane_b32 s16, v6, 0
	v_readlane_b32 s18, v6, 1
	v_readlane_b32 s20, v6, 2
	v_readlane_b32 s22, v6, 3
	v_readlane_b32 s24, v6, 4
	v_readlane_b32 s26, v6, 5
	v_readlane_b32 s28, v6, 6
	v_readlane_b32 s30, v6, 7
	s_mov_b32 s66, s52
	s_lshl_b32 s67, s66, 12
	s_add_u32 s68, s62, s67
	s_addc_u32 s69, s63, 0
	global_load_dwordx4 v[176:179], v1, s[68:69] nt
	global_load_dwordx4 v[180:183], v1, s[68:69] offset:16 nt
	global_load_dwordx4 v[184:187], v1, s[68:69] offset:2048 nt
	global_load_dwordx4 v[188:191], v1, s[68:69] offset:2064 nt
	s_add_u32 s67, s66, 0x10000
	s_lshl_b32 s67, s67, 11
	s_add_u32 s68, s60, s67
	s_addc_u32 s69, s61, 0
	global_load_dwordx4 v[104:107], v0, s[68:69] nt
	global_load_dwordx4 v[108:111], v0, s[68:69] offset:1024 nt
	s_lshl_b32 s67, s70, 11
	s_add_u32 s68, s60, s67
	s_addc_u32 s69, s61, 0
	global_load_dwordx4 v[112:115], v0, s[68:69] nt
	global_load_dwordx4 v[116:119], v0, s[68:69] offset:1024 nt
	s_lshl_b32 s67, s71, 11
	s_add_u32 s68, s60, s67
	s_addc_u32 s69, s61, 0
	global_load_dwordx4 v[120:123], v0, s[68:69] nt
	global_load_dwordx4 v[124:127], v0, s[68:69] offset:1024 nt
	s_lshl_b32 s67, s72, 11
	s_add_u32 s68, s60, s67
	s_addc_u32 s69, s61, 0
	global_load_dwordx4 v[128:131], v0, s[68:69] nt
	global_load_dwordx4 v[132:135], v0, s[68:69] offset:1024 nt
	s_lshl_b32 s67, s73, 11
	s_add_u32 s68, s60, s67
	s_addc_u32 s69, s61, 0
	global_load_dwordx4 v[136:139], v0, s[68:69] nt
	global_load_dwordx4 v[140:143], v0, s[68:69] offset:1024 nt
	s_lshl_b32 s67, s74, 11
	s_add_u32 s68, s60, s67
	s_addc_u32 s69, s61, 0
	global_load_dwordx4 v[144:147], v0, s[68:69] nt
	global_load_dwordx4 v[148:151], v0, s[68:69] offset:1024 nt
	s_lshl_b32 s67, s75, 11
	s_add_u32 s68, s60, s67
	s_addc_u32 s69, s61, 0
	global_load_dwordx4 v[152:155], v0, s[68:69] nt
	global_load_dwordx4 v[156:159], v0, s[68:69] offset:1024 nt
	s_lshl_b32 s67, s76, 11
	s_add_u32 s68, s60, s67
	s_addc_u32 s69, s61, 0
	global_load_dwordx4 v[160:163], v0, s[68:69] nt
	global_load_dwordx4 v[164:167], v0, s[68:69] offset:1024 nt
	s_lshl_b32 s67, s77, 11
	s_add_u32 s68, s60, s67
	s_addc_u32 s69, s61, 0
	global_load_dwordx4 v[168:171], v0, s[68:69] nt
	global_load_dwordx4 v[172:175], v0, s[68:69] offset:1024 nt
.Lcomb_sk7:
	s_mov_b32 s78, s52
	s_mov_b32 s52, s79
	s_add_u32 s79, s78, s53
	s_cmp_lt_u32 s79, 0x2000
	s_cbranch_scc0 .Lcomb_sk8
	s_mov_b32 s66, s79
	s_lshl_b32 s66, s66, 5
	s_add_u32 s68, s54, s66
	s_addc_u32 s69, s55, 0
	global_load_dword v4, v3, s[68:69]
	s_add_u32 s68, s56, s66
	s_addc_u32 s69, s57, 0
	global_load_dword v5, v3, s[68:69]
	s_add_u32 s68, s58, s66
	s_addc_u32 s69, s59, 0
	global_load_dword v6, v3, s[68:69]

.Lcomb_done:
.LBB0_2177:
	s_endpgm
